# prologue: helper CUs take half of the x conversion rows (16/wave), transposing CUs 5-6 rows/wave
# speedup vs baseline: 1.0191x; 1.0036x over previous
.LBB0_898:
	s_lshl_b32 s8, s43, 3
	s_add_i32 s8, s8, s91
	s_lshl_b32 s10, s42, 3
	s_movk_i32 s99, 0x3fff
	s_cmp_lg_u32 s42, 0x100
	s_cbranch_scc1 .Lp0_xs_done
	s_and_b32 s98, s43, 31
	s_lshr_b32 s8, s43, 5
	s_cmp_lt_u32 s98, 8
	s_cbranch_scc1 .Lp0_xs_B
	s_mul_i32 s8, s8, 24
	s_add_i32 s8, s8, s98
	s_add_i32 s8, s8, -8
	s_lshl_b32 s8, s8, 3
	s_add_i32 s8, s8, s91
	s_addk_i32 s8, 0x2000
	s_movk_i32 s10, 0x600
	s_branch .Lp0_xs_done
.Lp0_xs_B:
	s_lshl_b32 s8, s8, 3
	s_add_i32 s8, s8, s98
	s_lshl_b32 s8, s8, 3
	s_add_i32 s8, s8, s91
	s_movk_i32 s10, 0x200
	s_movk_i32 s99, 0x1fff

.LBB0_908:
	s_or_b64 exec, exec, s[2:3]
	s_cmp_gt_i32 s8, s99
	v_mbcnt_lo_u32_b32 v0, -1, 0
	v_mbcnt_hi_u32_b32 v0, -1, v0
	s_cbranch_scc1 .LBB0_913
	v_and_b32_e32 v4, 63, v0
	s_ashr_i32 s9, s8, 31
	s_waitcnt lgkmcnt(0)
	s_lshl_b64 s[4:5], s[8:9], 7
	v_lshlrev_b32_e32 v6, 2, v4
	v_mov_b32_e32 v7, 0
	v_lshl_add_u64 v[0:1], s[4:5], 0, v[6:7]
	s_mov_b64 s[4:5], 0x600000
	v_lshl_add_u64 v[0:1], v[0:1], 0, s[4:5]
	s_lshl_b64 s[4:5], s[8:9], 13
	v_lshl_or_b32 v2, v4, 4, s4
	v_mov_b32_e32 v3, s5
	s_lshl_b64 s[4:5], s[8:9], 12
	v_cmp_gt_u32_e32 vcc, 32, v4
	v_cmp_eq_u32_e64 s[2:3], 0, v4
	s_ashr_i32 s11, s10, 31
	v_lshl_or_b32 v4, v4, 3, s4
	v_mov_b32_e32 v5, s5
	s_lshl_b64 s[4:5], s[8:9], 11
	s_lshl_b64 s[14:15], s[10:11], 7
	v_or_b32_e32 v2, 0x1000, v2
	s_lshl_b64 s[16:17], s[10:11], 13
	s_lshl_b64 s[18:19], s[10:11], 12
	v_or_b32_e32 v6, s4, v6
	v_mov_b32_e32 v7, s5
	s_lshl_b64 s[20:21], s[10:11], 11
	s_movk_i32 s1, 0x7fff
	s_mov_b32 s9, 0x2d000000
	s_brev_b32 s11, 26
	v_mov_b32_e32 v12, 1
	s_branch .LBB0_911
.LBB0_910:
	s_or_b64 exec, exec, s[4:5]
	s_add_i32 s8, s8, s10
	v_lshl_add_u64 v[0:1], v[0:1], 0, s[14:15]
	v_lshl_add_u64 v[2:3], v[2:3], 0, s[16:17]
	v_lshl_add_u64 v[4:5], v[4:5], 0, s[18:19]
	s_cmp_gt_i32 s8, s99
	v_lshl_add_u64 v[6:7], v[6:7], 0, s[20:21]
	s_cbranch_scc1 .LBB0_913
